# P4: first key-fragment loads of both selection passes issued before the preceding Q-wait/barrier/LDS-clear instead of after them
# baseline (speedup 1.0000x reference)
; __device__ __forceinline__ bf16 f2bf(float f) { unsigned u = __float_as_uint(f); return (bf16)((u + 0x7fffu + ((u >> 16) & 1u)) >> 16); }
; #define DSA2_LOADK(dst, kt_) do { _Pragma("unroll") for (int s = 0; s < 4; ++s) dst[s] = *(const bf16x8*)(kp + (size_t)(32 * (kt_)) * Y0P + 16 * s); } while (0)
; template <int STAGE>
; __device__ __forceinline__ void pass2(LAS unsigned char* lds, const bf16* kbase, int g, int t0, const bf16x8 (&qf)[4][4], const f32x4 lo4, const f32x4 hi4, int wave, int r, int h2) {
;     ...
;     int kt = wave;
;     if (kt <= g) DSA2_LOADK(kf, kt);
; __device__ __forceinline__ bool run_unit2(LAS unsigned char* lds, const bf16* y0, const float* aux, unsigned* maskg, int b, int g, int tid_in, int wave, int lane) {
;     ...
;     bf16x8 qf[4][4];
;     {
;         const bf16* qp = y0 + (rowbase + t0 + r) * (size_t)Y0P + Y0_IQ + 8 * h2;
; #pragma unroll
;         for (int hd = 0; hd < 4; ++hd)
; #pragma unroll
;             for (int s = 0; s < 4; ++s) qf[hd][s] = *(const bf16x8*)(qp + hd * 64 + 16 * s);
;     }
;     const f32x4 w4 = *(const f32x4*)(aux + (rowbase + t0 + r) * 16 + 8);
;     f32x4 lo4, hi4;
; #pragma unroll
;     for (int hd = 0; hd < 4; ++hd) {
;         const float wsc = w4[hd] * 0.0625f;
;         lo4[hd] = (w4[hd] >= 0.f) ? 0.f : -INFINITY; hi4[hd] = (w4[hd] >= 0.f) ? INFINITY : 0.f;
; #pragma unroll
;         for (int s = 0; s < 4; ++s) {
;             bf16x8 a = qf[hd][s];
; #pragma unroll
;             for (int j = 0; j < 8; ++j) a[j] = (short)f2bf(__uint_as_float(((unsigned)(unsigned short)a[j]) << 16) * wsc);
;             qf[hd][s] = a;
;         }
;     }
;     const bf16* kbase = y0 + rowbase * (size_t)Y0P + Y0_IK;
;     __syncthreads();
.LBB0_779:
	s_or_b64 exec, exec, s[2:3]
	v_cmp_gt_i32_e32 vcc, 32, v206
	s_and_saveexec_b64 s[2:3], vcc
	v_lshl_add_u32 v0, v206, 2, 0
	v_add_u32_e32 v0, 0x18200, v0
	ds_write_b32 v0, v177
	s_or_b64 exec, exec, s[2:3]
	v_cmp_eq_u32_e32 vcc, 0, v206
	s_and_saveexec_b64 s[2:3], vcc
	v_mov_b32_e32 v0, s88
	ds_write_b32 v0, v177
	s_or_b64 exec, exec, s[2:3]
	s_andn2_b32 s64, 0xff, s0
	s_lshr_b32 s66, s0, 8
	v_and_b32_e32 v218, 31, v217
	s_lshl_b32 s41, s64, 5
	v_ashrrev_i32_e32 v219, 5, v217
	s_lshl_b64 s[76:77], s[66:67], 13
	v_or_b32_e32 v211, s41, v218
	v_or_b32_e32 v0, s76, v211
	v_mov_b64_e32 v[2:3], s[44:45]
	s_waitcnt vmcnt(0)
	v_lshlrev_b32_e32 v48, 3, v219
	v_mov_b32_e32 v1, s77
	v_mad_u64_u32 v[2:3], s[0:1], v0, s33, v[2:3]
	v_ashrrev_i32_e32 v49, 31, v48
	v_mad_u32_u24 v3, s77, v187, v3
	v_lshlrev_b64 v[50:51], 1, v[48:49]
	v_lshlrev_b64 v[0:1], 6, v[0:1]
	v_lshl_add_u64 v[2:3], v[2:3], 0, v[50:51]
	v_lshl_add_u64 v[0:1], s[46:47], 0, v[0:1]
	global_load_dwordx4 v[16:19], v[0:1], off offset:32
	v_add_co_u32_e32 v0, vcc, s31, v2
	s_mul_i32 s78, s66, 0x3800000
	s_nop 0
	v_addc_co_u32_e32 v1, vcc, 0, v3, vcc
	global_load_dwordx4 v[52:55], v[0:1], off offset:2048
	v_lshl_add_u64 v[0:1], v[2:3], 0, s[28:29]
	global_load_dwordx4 v[56:59], v[0:1], off offset:32
	global_load_dwordx4 v[60:63], v[0:1], off offset:64
	global_load_dwordx4 v[76:79], v[0:1], off offset:96
	global_load_dwordx4 v[80:83], v[0:1], off offset:128
	global_load_dwordx4 v[44:47], v[0:1], off offset:160
	global_load_dwordx4 v[40:43], v[0:1], off offset:192
	global_load_dwordx4 v[36:39], v[0:1], off offset:224
	global_load_dwordx4 v[32:35], v[0:1], off offset:256
	global_load_dwordx4 v[28:31], v[0:1], off offset:288
	global_load_dwordx4 v[24:27], v[0:1], off offset:320
	global_load_dwordx4 v[20:23], v[0:1], off offset:352
	global_load_dwordx4 v[12:15], v[0:1], off offset:384
	global_load_dwordx4 v[8:11], v[0:1], off offset:416
	global_load_dwordx4 v[4:7], v[0:1], off offset:448
	s_nop 0
	global_load_dwordx4 v[0:3], v[0:1], off offset:480
	s_mul_hi_u32 s79, s66, 0x3800000
	s_add_u32 s0, s44, s78
	s_addc_u32 s1, s45, s79
	s_add_u32 s80, s0, 0x1a00
	s_addc_u32 s81, s1, 0
	v_mul_u32_u24_e32 v176, 0x1c00, v218
	v_readlane_b32 s0, v254, 24
	s_cmp_le_u32 s0, s64
	s_cselect_b64 s[82:83], -1, 0
	s_cmp_gt_u32 s0, s64
	v_lshl_add_u64 v[180:181], s[80:81], 0, v[176:177]
	v_lshl_add_u64 v[180:181], v[180:181], 0, v[50:51]
	v_lshl_add_u64 v[180:181], v[180:181], 0, s[36:37]
	global_load_dwordx4 v[140:143], v[180:181], off
	global_load_dwordx4 v[136:139], v[180:181], off offset:32
	global_load_dwordx4 v[132:135], v[180:181], off offset:64
	global_load_dwordx4 v[128:131], v[180:181], off offset:96
	s_waitcnt lgkmcnt(0)
	s_barrier
	s_waitcnt vmcnt(4)
	v_and_b32_e32 v71, 0xffff0000, v57
	v_lshlrev_b32_e32 v70, 16, v57
	v_and_b32_e32 v57, 0xffff0000, v58
	v_and_b32_e32 v73, 0xffff0000, v59
	v_lshlrev_b32_e32 v72, 16, v59
	v_mul_f32_e32 v84, 0x3d800000, v16
	v_cmp_le_f32_e32 vcc, 0, v16
	v_and_b32_e32 v65, 0xffff0000, v52
	v_lshlrev_b32_e32 v64, 16, v52
	v_and_b32_e32 v67, 0xffff0000, v53
	v_lshlrev_b32_e32 v66, 16, v53
	v_and_b32_e32 v53, 0xffff0000, v54
	v_lshlrev_b32_e32 v52, 16, v54
	v_and_b32_e32 v69, 0xffff0000, v55
	v_lshlrev_b32_e32 v68, 16, v55
	v_and_b32_e32 v55, 0xffff0000, v56
	v_lshlrev_b32_e32 v54, 16, v56
	v_lshlrev_b32_e32 v56, 16, v58
	v_pk_mul_f32 v[58:59], v[84:85], v[64:65] op_sel_hi:[0,1]
	v_pk_mul_f32 v[64:65], v[84:85], v[66:67] op_sel_hi:[0,1]
	v_pk_mul_f32 v[52:53], v[84:85], v[52:53] op_sel_hi:[0,1]
	v_pk_mul_f32 v[66:67], v[84:85], v[68:69] op_sel_hi:[0,1]
	v_pk_mul_f32 v[54:55], v[84:85], v[54:55] op_sel_hi:[0,1]
	v_pk_mul_f32 v[68:69], v[84:85], v[70:71] op_sel_hi:[0,1]
	v_pk_mul_f32 v[56:57], v[84:85], v[56:57] op_sel_hi:[0,1]
	v_pk_mul_f32 v[70:71], v[84:85], v[72:73] op_sel_hi:[0,1]
	v_bfe_u32 v16, v67, 16, 1
	v_bfe_u32 v72, v66, 16, 1
	v_bfe_u32 v73, v53, 16, 1
	v_bfe_u32 v74, v52, 16, 1
	v_bfe_u32 v75, v65, 16, 1
	v_bfe_u32 v85, v64, 16, 1
	v_bfe_u32 v86, v59, 16, 1
	v_bfe_u32 v87, v58, 16, 1
	v_add3_u32 v58, v58, v87, s73
	v_add3_u32 v59, v59, v86, s73
	v_add3_u32 v64, v64, v85, s73
	v_add3_u32 v65, v65, v75, s73
	v_add3_u32 v52, v52, v74, s73
	v_add3_u32 v53, v53, v73, s73
	v_add3_u32 v66, v66, v72, s73
	v_add3_u32 v16, v67, v16, s73
	v_bfe_u32 v88, v71, 16, 1
	v_bfe_u32 v89, v70, 16, 1
	v_bfe_u32 v90, v57, 16, 1
	v_bfe_u32 v91, v56, 16, 1
	v_perm_b32 v67, v16, v66, s72
	v_perm_b32 v66, v53, v52, s72
	v_perm_b32 v65, v65, v64, s72
	v_perm_b32 v64, v59, v58, s72
	v_bfe_u32 v16, v69, 16, 1
	v_bfe_u32 v52, v68, 16, 1
	v_bfe_u32 v53, v55, 16, 1
	v_bfe_u32 v58, v54, 16, 1
	v_add3_u32 v54, v54, v58, s73
	v_add3_u32 v53, v55, v53, s73
	v_add3_u32 v52, v68, v52, s73
	v_add3_u32 v16, v69, v16, s73
	v_add3_u32 v55, v56, v91, s73
	v_add3_u32 v56, v57, v90, s73
	v_add3_u32 v57, v70, v89, s73
	v_add3_u32 v58, v71, v88, s73
	v_perm_b32 v71, v58, v57, s72
	v_perm_b32 v70, v56, v55, s72
	v_perm_b32 v69, v16, v52, s72
	v_perm_b32 v68, v53, v54, s72
	v_and_b32_e32 v53, 0xffff0000, v60
	v_lshlrev_b32_e32 v52, 16, v60
	v_and_b32_e32 v55, 0xffff0000, v61
	v_lshlrev_b32_e32 v54, 16, v61
	v_and_b32_e32 v57, 0xffff0000, v62
	v_lshlrev_b32_e32 v56, 16, v62
	v_and_b32_e32 v59, 0xffff0000, v63
	v_lshlrev_b32_e32 v58, 16, v63
	v_pk_mul_f32 v[52:53], v[84:85], v[52:53] op_sel_hi:[0,1]
	v_pk_mul_f32 v[54:55], v[84:85], v[54:55] op_sel_hi:[0,1]
	v_pk_mul_f32 v[56:57], v[84:85], v[56:57] op_sel_hi:[0,1]
	v_pk_mul_f32 v[58:59], v[84:85], v[58:59] op_sel_hi:[0,1]
	v_bfe_u32 v16, v59, 16, 1
	v_bfe_u32 v60, v58, 16, 1
	v_bfe_u32 v61, v57, 16, 1
	v_bfe_u32 v62, v56, 16, 1
	v_bfe_u32 v63, v55, 16, 1
; __device__ __forceinline__ bf16 f2bf(float f) { unsigned u = __float_as_uint(f); return (bf16)((u + 0x7fffu + ((u >> 16) & 1u)) >> 16); }
; __device__ __forceinline__ bool run_unit2(LAS unsigned char* lds, const bf16* y0, const float* aux, unsigned* maskg, int b, int g, int tid_in, int wave, int lane) {
;     ...
;     for (int hd = 0; hd < 4; ++hd) {
;         const float wsc = w4[hd] * 0.0625f;
;         lo4[hd] = (w4[hd] >= 0.f) ? 0.f : -INFINITY; hi4[hd] = (w4[hd] >= 0.f) ? INFINITY : 0.f;
; #pragma unroll
;         for (int s = 0; s < 4; ++s) {
;             bf16x8 a = qf[hd][s];
; #pragma unroll
;             for (int j = 0; j < 8; ++j) a[j] = (short)f2bf(__uint_as_float(((unsigned)(unsigned short)a[j]) << 16) * wsc);
;             qf[hd][s] = a;
;         }
;     }
	v_bfe_u32 v72, v54, 16, 1
	v_bfe_u32 v73, v53, 16, 1
	v_bfe_u32 v74, v52, 16, 1
	v_add3_u32 v52, v52, v74, s73
	v_add3_u32 v53, v53, v73, s73
	v_add3_u32 v54, v54, v72, s73
	v_add3_u32 v55, v55, v63, s73
	v_add3_u32 v56, v56, v62, s73
	v_add3_u32 v57, v57, v61, s73
	v_add3_u32 v58, v58, v60, s73
	v_add3_u32 v16, v59, v16, s73
	v_perm_b32 v75, v16, v58, s72
	v_perm_b32 v74, v57, v56, s72
	v_perm_b32 v73, v55, v54, s72
	v_perm_b32 v72, v53, v52, s72
	v_and_b32_e32 v53, 0xffff0000, v76
	v_lshlrev_b32_e32 v52, 16, v76
	v_and_b32_e32 v55, 0xffff0000, v77
	v_lshlrev_b32_e32 v54, 16, v77
	v_and_b32_e32 v57, 0xffff0000, v78
	v_lshlrev_b32_e32 v56, 16, v78
	v_and_b32_e32 v59, 0xffff0000, v79
	v_lshlrev_b32_e32 v58, 16, v79
	v_pk_mul_f32 v[52:53], v[84:85], v[52:53] op_sel_hi:[0,1]
	v_pk_mul_f32 v[54:55], v[84:85], v[54:55] op_sel_hi:[0,1]
	v_pk_mul_f32 v[56:57], v[84:85], v[56:57] op_sel_hi:[0,1]
	v_pk_mul_f32 v[58:59], v[84:85], v[58:59] op_sel_hi:[0,1]
	v_bfe_u32 v16, v59, 16, 1
	v_bfe_u32 v60, v58, 16, 1
	v_bfe_u32 v61, v57, 16, 1
	v_bfe_u32 v62, v56, 16, 1
	v_bfe_u32 v63, v55, 16, 1
	v_bfe_u32 v76, v54, 16, 1
	v_bfe_u32 v77, v53, 16, 1
	v_bfe_u32 v78, v52, 16, 1
	v_add3_u32 v52, v52, v78, s73
	v_add3_u32 v53, v53, v77, s73
	v_add3_u32 v54, v54, v76, s73
	v_add3_u32 v55, v55, v63, s73
	v_add3_u32 v56, v56, v62, s73
	v_add3_u32 v57, v57, v61, s73
	v_add3_u32 v58, v58, v60, s73
	v_add3_u32 v16, v59, v16, s73
	v_perm_b32 v79, v16, v58, s72
	v_perm_b32 v78, v57, v56, s72
	v_perm_b32 v77, v55, v54, s72
	v_perm_b32 v76, v53, v52, s72
	v_mul_f32_e32 v16, 0x3d800000, v17
	v_and_b32_e32 v53, 0xffff0000, v80
	v_lshlrev_b32_e32 v52, 16, v80
	v_and_b32_e32 v55, 0xffff0000, v81
	v_lshlrev_b32_e32 v54, 16, v81
	v_and_b32_e32 v57, 0xffff0000, v82
	v_lshlrev_b32_e32 v56, 16, v82
	v_pk_mul_f32 v[52:53], v[16:17], v[52:53] op_sel_hi:[0,1]
	v_pk_mul_f32 v[54:55], v[16:17], v[54:55] op_sel_hi:[0,1]
	v_pk_mul_f32 v[56:57], v[16:17], v[56:57] op_sel_hi:[0,1]
	v_and_b32_e32 v59, 0xffff0000, v83
	v_lshlrev_b32_e32 v58, 16, v83
	v_pk_mul_f32 v[58:59], v[16:17], v[58:59] op_sel_hi:[0,1]
	v_bfe_u32 v61, v57, 16, 1
	v_bfe_u32 v62, v56, 16, 1
	v_bfe_u32 v63, v55, 16, 1
	v_bfe_u32 v80, v54, 16, 1
	v_bfe_u32 v81, v53, 16, 1
	v_bfe_u32 v82, v52, 16, 1
	v_cndmask_b32_e64 v207, v188, 0, vcc
	v_cndmask_b32_e32 v208, 0, v189, vcc
	v_cmp_le_f32_e32 vcc, 0, v17
	v_bfe_u32 v17, v59, 16, 1
	v_add3_u32 v52, v52, v82, s73
	v_add3_u32 v53, v53, v81, s73
	v_add3_u32 v54, v54, v80, s73
	v_add3_u32 v55, v55, v63, s73
	v_add3_u32 v56, v56, v62, s73
	v_add3_u32 v57, v57, v61, s73
	v_bfe_u32 v60, v58, 16, 1
	v_add3_u32 v17, v59, v17, s73
	v_perm_b32 v82, v57, v56, s72
	v_perm_b32 v81, v55, v54, s72
	v_perm_b32 v80, v53, v52, s72
	v_and_b32_e32 v53, 0xffff0000, v44
	v_lshlrev_b32_e32 v52, 16, v44
	v_and_b32_e32 v55, 0xffff0000, v45
	v_lshlrev_b32_e32 v54, 16, v45
	v_and_b32_e32 v57, 0xffff0000, v47
	v_lshlrev_b32_e32 v56, 16, v47
	v_add3_u32 v58, v58, v60, s73
	v_pk_mul_f32 v[52:53], v[16:17], v[52:53] op_sel_hi:[0,1]
	v_pk_mul_f32 v[44:45], v[16:17], v[54:55] op_sel_hi:[0,1]
	v_and_b32_e32 v55, 0xffff0000, v46
	v_lshlrev_b32_e32 v54, 16, v46
	v_pk_mul_f32 v[46:47], v[16:17], v[56:57] op_sel_hi:[0,1]
	v_perm_b32 v83, v17, v58, s72
	v_pk_mul_f32 v[54:55], v[16:17], v[54:55] op_sel_hi:[0,1]
	v_bfe_u32 v17, v47, 16, 1
	v_bfe_u32 v56, v46, 16, 1
	v_bfe_u32 v61, v53, 16, 1
	v_bfe_u32 v62, v52, 16, 1
	v_bfe_u32 v59, v45, 16, 1
	v_bfe_u32 v60, v44, 16, 1
	v_add3_u32 v52, v52, v62, s73
	v_add3_u32 v53, v53, v61, s73
	v_add3_u32 v46, v46, v56, s73
	v_add3_u32 v17, v47, v17, s73
	v_add3_u32 v44, v44, v60, s73
	v_add3_u32 v45, v45, v59, s73
	v_perm_b32 v87, v17, v46, s72
	v_perm_b32 v84, v53, v52, s72
	v_and_b32_e32 v47, 0xffff0000, v41
	v_lshlrev_b32_e32 v46, 16, v41
	v_and_b32_e32 v53, 0xffff0000, v43
	v_lshlrev_b32_e32 v52, 16, v43
	v_bfe_u32 v57, v55, 16, 1
	v_bfe_u32 v58, v54, 16, 1
	v_perm_b32 v85, v45, v44, s72
	v_and_b32_e32 v45, 0xffff0000, v40
	v_lshlrev_b32_e32 v44, 16, v40
	v_pk_mul_f32 v[40:41], v[16:17], v[46:47] op_sel_hi:[0,1]
	v_and_b32_e32 v47, 0xffff0000, v42
	v_lshlrev_b32_e32 v46, 16, v42
	v_pk_mul_f32 v[42:43], v[16:17], v[52:53] op_sel_hi:[0,1]
	v_add3_u32 v54, v54, v58, s73
	v_add3_u32 v55, v55, v57, s73
	v_pk_mul_f32 v[44:45], v[16:17], v[44:45] op_sel_hi:[0,1]
	v_pk_mul_f32 v[46:47], v[16:17], v[46:47] op_sel_hi:[0,1]
	v_bfe_u32 v17, v43, 16, 1
	v_bfe_u32 v52, v42, 16, 1
	v_perm_b32 v86, v55, v54, s72
	v_bfe_u32 v55, v41, 16, 1
	v_bfe_u32 v56, v40, 16, 1
	v_bfe_u32 v57, v45, 16, 1
	v_bfe_u32 v58, v44, 16, 1
	v_add3_u32 v42, v42, v52, s73
	v_add3_u32 v17, v43, v17, s73
	v_add3_u32 v44, v44, v58, s73
	v_add3_u32 v45, v45, v57, s73
	v_add3_u32 v40, v40, v56, s73
	v_add3_u32 v41, v41, v55, s73
	v_perm_b32 v91, v17, v42, s72
	v_and_b32_e32 v43, 0xffff0000, v37
	v_lshlrev_b32_e32 v42, 16, v37
	v_perm_b32 v89, v41, v40, s72
	v_perm_b32 v88, v45, v44, s72
	v_and_b32_e32 v41, 0xffff0000, v36
	v_lshlrev_b32_e32 v40, 16, v36
	v_pk_mul_f32 v[36:37], v[16:17], v[42:43] op_sel_hi:[0,1]
	v_and_b32_e32 v43, 0xffff0000, v38
	v_lshlrev_b32_e32 v42, 16, v38
	v_and_b32_e32 v45, 0xffff0000, v39
	v_lshlrev_b32_e32 v44, 16, v39
	v_bfe_u32 v53, v47, 16, 1
	v_bfe_u32 v54, v46, 16, 1
	v_pk_mul_f32 v[40:41], v[16:17], v[40:41] op_sel_hi:[0,1]
	v_pk_mul_f32 v[42:43], v[16:17], v[42:43] op_sel_hi:[0,1]
	v_pk_mul_f32 v[16:17], v[16:17], v[44:45] op_sel_hi:[0,1]
	v_add3_u32 v46, v46, v54, s73
	v_add3_u32 v47, v47, v53, s73
	v_bfe_u32 v38, v17, 16, 1
	v_bfe_u32 v39, v16, 16, 1
	v_perm_b32 v90, v47, v46, s72
	v_bfe_u32 v46, v37, 16, 1
	v_bfe_u32 v47, v36, 16, 1
	v_bfe_u32 v52, v41, 16, 1
	v_bfe_u32 v53, v40, 16, 1
; __device__ __forceinline__ bf16 f2bf(float f) { unsigned u = __float_as_uint(f); return (bf16)((u + 0x7fffu + ((u >> 16) & 1u)) >> 16); }
; __device__ __forceinline__ bool run_unit2(LAS unsigned char* lds, const bf16* y0, const float* aux, unsigned* maskg, int b, int g, int tid_in, int wave, int lane) {
;     ...
;     for (int hd = 0; hd < 4; ++hd) {
;         const float wsc = w4[hd] * 0.0625f;
;         lo4[hd] = (w4[hd] >= 0.f) ? 0.f : -INFINITY; hi4[hd] = (w4[hd] >= 0.f) ? INFINITY : 0.f;
; #pragma unroll
;         for (int s = 0; s < 4; ++s) {
;             bf16x8 a = qf[hd][s];
; #pragma unroll
;             for (int j = 0; j < 8; ++j) a[j] = (short)f2bf(__uint_as_float(((unsigned)(unsigned short)a[j]) << 16) * wsc);
;             qf[hd][s] = a;
;         }
;     }
	v_add3_u32 v16, v16, v39, s73
	v_add3_u32 v17, v17, v38, s73
	v_bfe_u32 v44, v43, 16, 1
	v_bfe_u32 v45, v42, 16, 1
	v_add3_u32 v40, v40, v53, s73
	v_add3_u32 v41, v41, v52, s73
	v_add3_u32 v36, v36, v47, s73
	v_add3_u32 v37, v37, v46, s73
	v_perm_b32 v95, v17, v16, s72
	v_mul_f32_e32 v16, 0x3d800000, v18
	v_and_b32_e32 v39, 0xffff0000, v33
	v_lshlrev_b32_e32 v38, 16, v33
	v_add3_u32 v42, v42, v45, s73
	v_add3_u32 v43, v43, v44, s73
	v_perm_b32 v93, v37, v36, s72
	v_perm_b32 v92, v41, v40, s72
	v_and_b32_e32 v37, 0xffff0000, v32
	v_lshlrev_b32_e32 v36, 16, v32
	v_pk_mul_f32 v[32:33], v[16:17], v[38:39] op_sel_hi:[0,1]
	v_and_b32_e32 v41, 0xffff0000, v35
	v_lshlrev_b32_e32 v40, 16, v35
	v_perm_b32 v94, v43, v42, s72
	v_pk_mul_f32 v[36:37], v[16:17], v[36:37] op_sel_hi:[0,1]
	v_and_b32_e32 v39, 0xffff0000, v34
	v_lshlrev_b32_e32 v38, 16, v34
	v_pk_mul_f32 v[34:35], v[16:17], v[40:41] op_sel_hi:[0,1]
	v_bfe_u32 v42, v33, 16, 1
	v_bfe_u32 v43, v32, 16, 1
	v_cndmask_b32_e64 v209, v188, 0, vcc
	v_cndmask_b32_e32 v210, 0, v189, vcc
	v_cmp_le_f32_e32 vcc, 0, v18
	v_pk_mul_f32 v[38:39], v[16:17], v[38:39] op_sel_hi:[0,1]
	v_bfe_u32 v17, v35, 16, 1
	v_bfe_u32 v18, v34, 16, 1
	v_bfe_u32 v44, v37, 16, 1
	v_bfe_u32 v45, v36, 16, 1
	v_add3_u32 v32, v32, v43, s73
	v_add3_u32 v33, v33, v42, s73
	v_bfe_u32 v40, v39, 16, 1
	v_bfe_u32 v41, v38, 16, 1
	v_add3_u32 v36, v36, v45, s73
	v_add3_u32 v37, v37, v44, s73
	v_add3_u32 v18, v34, v18, s73
	v_add3_u32 v17, v35, v17, s73
	v_perm_b32 v97, v33, v32, s72
	v_and_b32_e32 v33, 0xffff0000, v28
	v_lshlrev_b32_e32 v32, 16, v28
	v_and_b32_e32 v35, 0xffff0000, v29
	v_lshlrev_b32_e32 v34, 16, v29
	v_add3_u32 v38, v38, v41, s73
	v_add3_u32 v39, v39, v40, s73
	v_perm_b32 v96, v37, v36, s72
	v_pk_mul_f32 v[32:33], v[16:17], v[32:33] op_sel_hi:[0,1]
	v_pk_mul_f32 v[28:29], v[16:17], v[34:35] op_sel_hi:[0,1]
	v_and_b32_e32 v37, 0xffff0000, v31
	v_lshlrev_b32_e32 v36, 16, v31
	v_perm_b32 v98, v39, v38, s72
	v_and_b32_e32 v35, 0xffff0000, v30
	v_lshlrev_b32_e32 v34, 16, v30
	v_pk_mul_f32 v[30:31], v[16:17], v[36:37] op_sel_hi:[0,1]
	v_bfe_u32 v38, v29, 16, 1
	v_bfe_u32 v39, v28, 16, 1
	v_bfe_u32 v40, v33, 16, 1
	v_bfe_u32 v41, v32, 16, 1
	v_perm_b32 v99, v17, v18, s72
	v_pk_mul_f32 v[34:35], v[16:17], v[34:35] op_sel_hi:[0,1]
	v_bfe_u32 v17, v31, 16, 1
	v_bfe_u32 v18, v30, 16, 1
	v_add3_u32 v32, v32, v41, s73
	v_add3_u32 v33, v33, v40, s73
	v_add3_u32 v28, v28, v39, s73
	v_add3_u32 v29, v29, v38, s73
	v_bfe_u32 v36, v35, 16, 1
	v_bfe_u32 v37, v34, 16, 1
	v_add3_u32 v18, v30, v18, s73
	v_add3_u32 v17, v31, v17, s73
	v_perm_b32 v101, v29, v28, s72
	v_perm_b32 v100, v33, v32, s72
	v_and_b32_e32 v29, 0xffff0000, v24
	v_lshlrev_b32_e32 v28, 16, v24
	v_and_b32_e32 v31, 0xffff0000, v25
	v_lshlrev_b32_e32 v30, 16, v25
	v_and_b32_e32 v33, 0xffff0000, v27
	v_lshlrev_b32_e32 v32, 16, v27
	v_add3_u32 v34, v34, v37, s73
	v_add3_u32 v35, v35, v36, s73
	v_pk_mul_f32 v[28:29], v[16:17], v[28:29] op_sel_hi:[0,1]
	v_pk_mul_f32 v[24:25], v[16:17], v[30:31] op_sel_hi:[0,1]
	v_and_b32_e32 v31, 0xffff0000, v26
	v_lshlrev_b32_e32 v30, 16, v26
	v_pk_mul_f32 v[26:27], v[16:17], v[32:33] op_sel_hi:[0,1]
	v_perm_b32 v103, v17, v18, s72
	v_perm_b32 v102, v35, v34, s72
	v_pk_mul_f32 v[30:31], v[16:17], v[30:31] op_sel_hi:[0,1]
	v_bfe_u32 v17, v27, 16, 1
	v_bfe_u32 v18, v26, 16, 1
	v_bfe_u32 v34, v25, 16, 1
	v_bfe_u32 v35, v24, 16, 1
	v_bfe_u32 v36, v29, 16, 1
	v_bfe_u32 v37, v28, 16, 1
	v_add3_u32 v28, v28, v37, s73
	v_add3_u32 v29, v29, v36, s73
	v_add3_u32 v24, v24, v35, s73
	v_add3_u32 v25, v25, v34, s73
	v_add3_u32 v18, v26, v18, s73
	v_add3_u32 v17, v27, v17, s73
	v_and_b32_e32 v27, 0xffff0000, v21
	v_lshlrev_b32_e32 v26, 16, v21
	v_bfe_u32 v32, v31, 16, 1
	v_bfe_u32 v33, v30, 16, 1
	v_perm_b32 v105, v25, v24, s72
	v_perm_b32 v104, v29, v28, s72
	v_and_b32_e32 v25, 0xffff0000, v20
	v_lshlrev_b32_e32 v24, 16, v20
	v_pk_mul_f32 v[20:21], v[16:17], v[26:27] op_sel_hi:[0,1]
	v_and_b32_e32 v27, 0xffff0000, v22
	v_lshlrev_b32_e32 v26, 16, v22
	v_and_b32_e32 v29, 0xffff0000, v23
	v_lshlrev_b32_e32 v28, 16, v23
	v_add3_u32 v30, v30, v33, s73
	v_add3_u32 v31, v31, v32, s73
	v_perm_b32 v107, v17, v18, s72
	v_pk_mul_f32 v[24:25], v[16:17], v[24:25] op_sel_hi:[0,1]
	v_pk_mul_f32 v[26:27], v[16:17], v[26:27] op_sel_hi:[0,1]
	v_pk_mul_f32 v[16:17], v[16:17], v[28:29] op_sel_hi:[0,1]
	v_perm_b32 v106, v31, v30, s72
	v_bfe_u32 v18, v17, 16, 1
	v_bfe_u32 v22, v16, 16, 1
	v_bfe_u32 v23, v27, 16, 1
	v_bfe_u32 v28, v26, 16, 1
	v_bfe_u32 v29, v21, 16, 1
	v_bfe_u32 v30, v20, 16, 1
	v_add3_u32 v20, v20, v30, s73
	v_add3_u32 v21, v21, v29, s73
	v_add3_u32 v26, v26, v28, s73
	v_add3_u32 v23, v27, v23, s73
	v_add3_u32 v16, v16, v22, s73
	v_add3_u32 v17, v17, v18, s73
	v_cndmask_b32_e64 v212, v188, 0, vcc
	v_cndmask_b32_e32 v213, 0, v189, vcc
	v_bfe_u32 v31, v25, 16, 1
	v_bfe_u32 v32, v24, 16, 1
	v_perm_b32 v111, v17, v16, s72
	v_perm_b32 v110, v23, v26, s72
; __device__ __forceinline__ bf16 f2bf(float f) { unsigned u = __float_as_uint(f); return (bf16)((u + 0x7fffu + ((u >> 16) & 1u)) >> 16); }
; #define DSA2_LOADK(dst, kt_) do { _Pragma("unroll") for (int s = 0; s < 4; ++s) dst[s] = *(const bf16x8*)(kp + (size_t)(32 * (kt_)) * Y0P + 16 * s); } while (0)
; template <int STAGE>
; __device__ __forceinline__ void pass2(LAS unsigned char* lds, const bf16* kbase, int g, int t0, const bf16x8 (&qf)[4][4], const f32x4 lo4, const f32x4 hi4, int wave, int r, int h2) {
;     ...
;     int kt = wave;
;     if (kt <= g) DSA2_LOADK(kf, kt);
; __device__ __forceinline__ bool run_unit2(LAS unsigned char* lds, const bf16* y0, const float* aux, unsigned* maskg, int b, int g, int tid_in, int wave, int lane) {
;     ...
;     for (int hd = 0; hd < 4; ++hd) {
;         const float wsc = w4[hd] * 0.0625f;
;         lo4[hd] = (w4[hd] >= 0.f) ? 0.f : -INFINITY; hi4[hd] = (w4[hd] >= 0.f) ? INFINITY : 0.f;
; #pragma unroll
;         for (int s = 0; s < 4; ++s) {
;             bf16x8 a = qf[hd][s];
; #pragma unroll
;             for (int j = 0; j < 8; ++j) a[j] = (short)f2bf(__uint_as_float(((unsigned)(unsigned short)a[j]) << 16) * wsc);
;             qf[hd][s] = a;
;         }
;     }
	v_perm_b32 v109, v21, v20, s72
	v_mul_f32_e32 v16, 0x3d800000, v19
	v_cmp_le_f32_e32 vcc, 0, v19
	v_and_b32_e32 v19, 0xffff0000, v12
	v_lshlrev_b32_e32 v18, 16, v12
	v_and_b32_e32 v21, 0xffff0000, v13
	v_lshlrev_b32_e32 v20, 16, v13
	v_and_b32_e32 v23, 0xffff0000, v15
	v_lshlrev_b32_e32 v22, 16, v15
	v_add3_u32 v24, v24, v32, s73
	v_add3_u32 v25, v25, v31, s73
	v_pk_mul_f32 v[18:19], v[16:17], v[18:19] op_sel_hi:[0,1]
	v_pk_mul_f32 v[12:13], v[16:17], v[20:21] op_sel_hi:[0,1]
	v_and_b32_e32 v21, 0xffff0000, v14
	v_lshlrev_b32_e32 v20, 16, v14
	v_pk_mul_f32 v[14:15], v[16:17], v[22:23] op_sel_hi:[0,1]
	v_perm_b32 v108, v25, v24, s72
	v_pk_mul_f32 v[20:21], v[16:17], v[20:21] op_sel_hi:[0,1]
	v_bfe_u32 v17, v15, 16, 1
	v_bfe_u32 v22, v14, 16, 1
	v_bfe_u32 v25, v13, 16, 1
	v_bfe_u32 v26, v12, 16, 1
	v_bfe_u32 v27, v19, 16, 1
	v_bfe_u32 v28, v18, 16, 1
	v_add3_u32 v18, v18, v28, s73
	v_add3_u32 v19, v19, v27, s73
	v_add3_u32 v12, v12, v26, s73
	v_add3_u32 v13, v13, v25, s73
	v_add3_u32 v14, v14, v22, s73
	v_add3_u32 v15, v15, v17, s73
	v_perm_b32 v115, v15, v14, s72
	v_perm_b32 v113, v13, v12, s72
	v_perm_b32 v112, v19, v18, s72
	v_and_b32_e32 v13, 0xffff0000, v8
	v_lshlrev_b32_e32 v12, 16, v8
	v_and_b32_e32 v15, 0xffff0000, v9
	v_lshlrev_b32_e32 v14, 16, v9
	v_and_b32_e32 v19, 0xffff0000, v11
	v_lshlrev_b32_e32 v18, 16, v11
	v_bfe_u32 v23, v21, 16, 1
	v_bfe_u32 v24, v20, 16, 1
	v_pk_mul_f32 v[12:13], v[16:17], v[12:13] op_sel_hi:[0,1]
	v_pk_mul_f32 v[8:9], v[16:17], v[14:15] op_sel_hi:[0,1]
	v_and_b32_e32 v15, 0xffff0000, v10
	v_lshlrev_b32_e32 v14, 16, v10
	v_pk_mul_f32 v[10:11], v[16:17], v[18:19] op_sel_hi:[0,1]
	v_add3_u32 v20, v20, v24, s73
	v_add3_u32 v21, v21, v23, s73
	v_pk_mul_f32 v[14:15], v[16:17], v[14:15] op_sel_hi:[0,1]
	v_bfe_u32 v17, v11, 16, 1
	v_bfe_u32 v18, v10, 16, 1
	v_bfe_u32 v23, v13, 16, 1
	v_bfe_u32 v24, v12, 16, 1
	v_perm_b32 v114, v21, v20, s72
	v_bfe_u32 v21, v9, 16, 1
	v_bfe_u32 v22, v8, 16, 1
	v_add3_u32 v12, v12, v24, s73
	v_add3_u32 v13, v13, v23, s73
	v_add3_u32 v10, v10, v18, s73
	v_add3_u32 v11, v11, v17, s73
	v_add3_u32 v8, v8, v22, s73
	v_add3_u32 v9, v9, v21, s73
	v_perm_b32 v119, v11, v10, s72
	v_perm_b32 v116, v13, v12, s72
	v_and_b32_e32 v11, 0xffff0000, v5
	v_lshlrev_b32_e32 v10, 16, v5
	v_and_b32_e32 v13, 0xffff0000, v7
	v_lshlrev_b32_e32 v12, 16, v7
	v_perm_b32 v117, v9, v8, s72
	v_and_b32_e32 v9, 0xffff0000, v4
	v_lshlrev_b32_e32 v8, 16, v4
	v_pk_mul_f32 v[4:5], v[16:17], v[10:11] op_sel_hi:[0,1]
	v_and_b32_e32 v11, 0xffff0000, v6
	v_lshlrev_b32_e32 v10, 16, v6
	v_pk_mul_f32 v[6:7], v[16:17], v[12:13] op_sel_hi:[0,1]
	v_bfe_u32 v19, v15, 16, 1
	v_bfe_u32 v20, v14, 16, 1
	v_pk_mul_f32 v[8:9], v[16:17], v[8:9] op_sel_hi:[0,1]
	v_bfe_u32 v12, v7, 16, 1
	v_bfe_u32 v13, v6, 16, 1
	v_add3_u32 v14, v14, v20, s73
	v_add3_u32 v15, v15, v19, s73
	v_pk_mul_f32 v[10:11], v[16:17], v[10:11] op_sel_hi:[0,1]
	v_bfe_u32 v17, v5, 16, 1
	v_bfe_u32 v18, v4, 16, 1
	v_bfe_u32 v19, v9, 16, 1
	v_bfe_u32 v20, v8, 16, 1
	v_add3_u32 v6, v6, v13, s73
	v_add3_u32 v7, v7, v12, s73
	v_add3_u32 v8, v8, v20, s73
	v_add3_u32 v9, v9, v19, s73
	v_add3_u32 v4, v4, v18, s73
	v_add3_u32 v5, v5, v17, s73
	v_perm_b32 v123, v7, v6, s72
	v_and_b32_e32 v7, 0xffff0000, v1
	v_lshlrev_b32_e32 v6, 16, v1
	v_perm_b32 v118, v15, v14, s72
	v_bfe_u32 v14, v11, 16, 1
	v_bfe_u32 v15, v10, 16, 1
	v_perm_b32 v121, v5, v4, s72
	v_perm_b32 v120, v9, v8, s72
	v_and_b32_e32 v5, 0xffff0000, v0
	v_lshlrev_b32_e32 v4, 16, v0
	v_pk_mul_f32 v[0:1], v[16:17], v[6:7] op_sel_hi:[0,1]
	v_and_b32_e32 v7, 0xffff0000, v2
	v_lshlrev_b32_e32 v6, 16, v2
	v_and_b32_e32 v9, 0xffff0000, v3
	v_lshlrev_b32_e32 v8, 16, v3
	v_add3_u32 v10, v10, v15, s73
	v_add3_u32 v11, v11, v14, s73
	v_pk_mul_f32 v[4:5], v[16:17], v[4:5] op_sel_hi:[0,1]
	v_pk_mul_f32 v[6:7], v[16:17], v[6:7] op_sel_hi:[0,1]
	v_pk_mul_f32 v[2:3], v[16:17], v[8:9] op_sel_hi:[0,1]
	v_bfe_u32 v12, v1, 16, 1
	v_bfe_u32 v13, v0, 16, 1
	v_perm_b32 v122, v11, v10, s72
	v_bfe_u32 v8, v3, 16, 1
	v_bfe_u32 v9, v2, 16, 1
	v_bfe_u32 v10, v7, 16, 1
	v_bfe_u32 v11, v6, 16, 1
	v_bfe_u32 v14, v5, 16, 1
	v_bfe_u32 v15, v4, 16, 1
	v_add3_u32 v0, v0, v13, s73
	v_add3_u32 v1, v1, v12, s73
	v_add3_u32 v4, v4, v15, s73
	v_add3_u32 v5, v5, v14, s73
	v_add3_u32 v6, v6, v11, s73
	v_add3_u32 v7, v7, v10, s73
	v_add3_u32 v2, v2, v9, s73
	v_add3_u32 v3, v3, v8, s73
	v_perm_b32 v125, v1, v0, s72
	v_lshl_add_u64 v[0:1], s[80:81], 0, v[176:177]
	v_cndmask_b32_e64 v214, v188, 0, vcc
	v_cndmask_b32_e32 v215, 0, v189, vcc
	v_perm_b32 v127, v3, v2, s72
	v_perm_b32 v126, v7, v6, s72
	v_perm_b32 v124, v5, v4, s72
	v_lshl_add_u64 v[178:179], v[0:1], 0, v[50:51]
	s_cbranch_scc1 .LBB0_804
	v_lshl_add_u64 v[0:1], v[48:49], 1, s[78:79]
	v_lshl_add_u64 v[0:1], v[0:1], 0, v[176:177]
	v_mad_u32_u24 v204, v218, s26, 0
	v_lshl_add_u64 v[180:181], s[34:35], 0, v[0:1]
	s_sub_i32 s0, 0, s64
	s_mov_b32 s1, s30
	s_mov_b32 s6, s92

; #define LAS __attribute__((address_space(3)))
; __device__ __forceinline__ bool run_unit2(LAS unsigned char* lds, const bf16* y0, const float* aux, unsigned* maskg, int b, int g, int tid_in, int wave, int lane) {
;     ...
;     pass2<0>(lds, kbase, g, t0, qf, lo4, hi4, wave, r, h2);
;     __syncthreads();
;     {
;         const int q = tid >> 4, i = tid & 15;
;         unsigned c[30]; unsigned cs = 0u;
; #pragma unroll
;         for (int k = 0; k < 30; ++k) { c[k] = hist[q * HROW2 + 30 * i + k]; cs += c[k]; }
;         unsigned v = cs;
; #pragma unroll
;         for (int o = 1; o < 16; o <<= 1) { const unsigned t = (unsigned)__shfl_down((int)v, o, 16); if (i + o < 16) v += t; }
;         const unsigned above = v - cs;
;         if (i == 0) { const bool selall = (t0 + q) < 256; if (selall || v < 256u) { ((LAS int*)(lds + OFF2_TB))[q] = -1; ((LAS int*)(lds + OFF2_NEED))[q] = 0; } }
;         if (!((t0 + q) < 256) && above < 256u && 256u <= above + cs) {
;             unsigned cum = above; bool done = false;
; #pragma unroll
;             for (int k = 29; k >= 0; --k) { if (!done) { if (cum + c[k] >= 256u) { ((LAS int*)(lds + OFF2_TB))[q] = 30 * i + k; ((LAS int*)(lds + OFF2_NEED))[q] = (int)(256u - cum);
;                         if (c[k] > (unsigned)CAP2) ((LAS int*)(lds + OFF2_FLAG))[0] = 1; done = true; } else cum += c[k]; } }
;         }
.LBB0_804:
	s_waitcnt vmcnt(0)
	v_ashrrev_i32_e32 v220, 4, v206
	v_and_b32_e32 v216, 15, v206
	v_mul_lo_u32 v0, v220, s26
	v_mul_u32_u24_e32 v1, 0x78, v216
	v_add3_u32 v28, 0, v0, v1
	s_waitcnt lgkmcnt(0)
	s_barrier
	ds_read2_b32 v[0:1], v28 offset1:1
	ds_read2_b32 v[2:3], v28 offset0:2 offset1:3
	ds_read2_b32 v[4:5], v28 offset0:4 offset1:5
	ds_read2_b32 v[6:7], v28 offset0:6 offset1:7
	v_and_b32_e32 v31, 15, v192
	s_waitcnt lgkmcnt(3)
	v_add_u32_e32 v8, v1, v0
	s_waitcnt lgkmcnt(2)
	v_add3_u32 v8, v8, v2, v3
	s_waitcnt lgkmcnt(1)
	v_add3_u32 v14, v8, v4, v5
	ds_read2_b32 v[8:9], v28 offset0:8 offset1:9
	ds_read2_b32 v[10:11], v28 offset0:10 offset1:11
	ds_read2_b32 v[12:13], v28 offset0:12 offset1:13
	s_waitcnt lgkmcnt(3)
	v_add3_u32 v16, v14, v6, v7
	ds_read2_b32 v[14:15], v28 offset0:14 offset1:15
	s_waitcnt lgkmcnt(3)
	v_add3_u32 v16, v16, v8, v9
	s_waitcnt lgkmcnt(2)
	v_add3_u32 v16, v16, v10, v11
	s_waitcnt lgkmcnt(1)
	v_add3_u32 v20, v16, v12, v13
	ds_read2_b32 v[16:17], v28 offset0:16 offset1:17
	ds_read2_b32 v[18:19], v28 offset0:18 offset1:19
	s_waitcnt lgkmcnt(2)
	v_add3_u32 v24, v20, v14, v15
	ds_read2_b32 v[20:21], v28 offset0:20 offset1:21
	ds_read2_b32 v[22:23], v28 offset0:22 offset1:23
	v_cmp_ne_u32_e32 vcc, 15, v31
	s_waitcnt lgkmcnt(3)
	v_add3_u32 v24, v24, v16, v17
	s_waitcnt lgkmcnt(2)
	v_add3_u32 v30, v24, v18, v19
	ds_read2_b32 v[24:25], v28 offset0:24 offset1:25
	ds_read2_b32 v[26:27], v28 offset0:26 offset1:27
	ds_read2_b32 v[28:29], v28 offset0:28 offset1:29
	s_waitcnt lgkmcnt(4)
	v_add3_u32 v30, v30, v20, v21
	s_waitcnt lgkmcnt(3)
	v_add3_u32 v30, v30, v22, v23
	s_waitcnt lgkmcnt(2)
	v_add3_u32 v30, v30, v24, v25
	s_waitcnt lgkmcnt(1)
	v_add3_u32 v30, v30, v26, v27
	v_addc_co_u32_e32 v31, vcc, 0, v192, vcc
	s_waitcnt lgkmcnt(0)
	v_add3_u32 v30, v30, v28, v29
	v_lshlrev_b32_e32 v180, 2, v31
	ds_bpermute_b32 v31, v180, v30
	v_bitop3_b32 v32, v192, 15, v192 bitop3:0xc
	v_cmp_ne_u32_e32 vcc, 15, v216
	v_lshl_add_u32 v221, v220, 2, 0
	s_waitcnt lgkmcnt(0)
	v_cndmask_b32_e32 v31, 0, v31, vcc
	v_cmp_gt_u32_e32 vcc, 2, v32
	v_add_u32_e32 v31, v31, v30
	s_nop 0
	v_cndmask_b32_e64 v33, 2, 0, vcc
	v_add_lshl_u32 v181, v33, v192, 2
	ds_bpermute_b32 v33, v181, v31
	v_cmp_gt_u32_e32 vcc, 14, v216
	s_waitcnt lgkmcnt(0)
	s_nop 0
	v_cndmask_b32_e32 v33, 0, v33, vcc
	v_cmp_gt_u32_e32 vcc, 4, v32
	v_add_u32_e32 v31, v33, v31
	s_nop 0
	v_cndmask_b32_e64 v32, 4, 0, vcc
	v_add_lshl_u32 v204, v32, v192, 2
	ds_bpermute_b32 v32, v204, v31
	v_cmp_gt_u32_e32 vcc, 12, v216
	s_waitcnt lgkmcnt(0)
	s_nop 0
	v_cndmask_b32_e32 v32, 0, v32, vcc
	v_add_u32_e32 v31, v32, v31
	v_bitop3_b32 v32, v192, 8, 15 bitop3:8
	v_add_lshl_u32 v205, v32, v192, 2
	ds_bpermute_b32 v32, v205, v31
	v_cmp_gt_u32_e32 vcc, 8, v216
	s_waitcnt lgkmcnt(0)
	s_nop 0
	v_cndmask_b32_e32 v32, 0, v32, vcc
	v_add_u32_e32 v31, v32, v31
	v_add_u32_e32 v32, s41, v220
	v_cmp_gt_i32_e64 s[2:3], s68, v32
	v_cmp_gt_u32_e64 s[4:5], s68, v31
	v_cmp_eq_u32_e32 vcc, 0, v216
	s_or_b64 s[0:1], s[2:3], s[4:5]
	s_and_b64 s[0:1], vcc, s[0:1]
	s_and_saveexec_b64 s[2:3], s[0:1]
	s_cbranch_execz .LBB0_806
	v_add_u32_e32 v34, 0x18100, v221
	v_add_u32_e32 v33, 0x18180, v221
	ds_write_b32 v34, v185
	ds_write_b32 v33, v177

; #define LAS __attribute__((address_space(3)))
; #define DSA2_LOADK(dst, kt_) do { _Pragma("unroll") for (int s = 0; s < 4; ++s) dst[s] = *(const bf16x8*)(kp + (size_t)(32 * (kt_)) * Y0P + 16 * s); } while (0)
; template <int STAGE>
; __device__ __forceinline__ void pass2(LAS unsigned char* lds, const bf16* kbase, int g, int t0, const bf16x8 (&qf)[4][4], const f32x4 lo4, const f32x4 hi4, int wave, int r, int h2) {
;     ...
;     int kt = wave;
;     if (kt <= g) DSA2_LOADK(kf, kt);
; __device__ __forceinline__ bool run_unit2(LAS unsigned char* lds, const bf16* y0, const float* aux, unsigned* maskg, int b, int g, int tid_in, int wave, int lane) {
;     ...
;     for (int i = tid; i < 65536 / 4; i += NTHR) ((LAS unsigned*)lds)[i] = 0u;
;     __syncthreads();
;     pass2<1>(lds, kbase, g, t0, qf, lo4, hi4, wave, r, h2);
.LBB0_818:
.LBB0_819:
	v_lshl_add_u64 v[0:1], v[178:179], 0, s[36:37]
	global_load_dwordx4 v[140:143], v[0:1], off
	global_load_dwordx4 v[136:139], v[0:1], off offset:32
	global_load_dwordx4 v[132:135], v[0:1], off offset:64
	global_load_dwordx4 v[128:131], v[0:1], off offset:96
	s_movk_i32 s0, 0x4000
	v_cmp_gt_i32_e32 vcc, s0, v206
	s_and_saveexec_b64 s[4:5], vcc
	s_cbranch_execz .LBB0_822
	v_lshl_add_u32 v1, v206, 2, 0
	ds_write2st64_b32 v1, v177, v177 offset0:0 offset1:8
	ds_write2st64_b32 v1, v177, v177 offset0:16 offset1:24
	ds_write2st64_b32 v1, v177, v177 offset0:32 offset1:40
	ds_write2st64_b32 v1, v177, v177 offset0:48 offset1:56
	ds_write2st64_b32 v1, v177, v177 offset0:64 offset1:72
	ds_write2st64_b32 v1, v177, v177 offset0:80 offset1:88
	ds_write2st64_b32 v1, v177, v177 offset0:96 offset1:104
	ds_write2st64_b32 v1, v177, v177 offset0:112 offset1:120
	ds_write2st64_b32 v1, v177, v177 offset0:128 offset1:136
	ds_write2st64_b32 v1, v177, v177 offset0:144 offset1:152
	ds_write2st64_b32 v1, v177, v177 offset0:160 offset1:168
	ds_write2st64_b32 v1, v177, v177 offset0:176 offset1:184
	ds_write2st64_b32 v1, v177, v177 offset0:192 offset1:200
	ds_write2st64_b32 v1, v177, v177 offset0:208 offset1:216
	ds_write2st64_b32 v1, v177, v177 offset0:224 offset1:232
	ds_write2st64_b32 v1, v177, v177 offset0:240 offset1:248
	s_movk_i32 s0, 0x3dff
	s_mov_b64 s[6:7], exec
.LBB0_822:
	s_or_b64 exec, exec, s[4:5]
	s_andn2_b64 vcc, exec, s[82:83]
	s_waitcnt lgkmcnt(0)
	s_barrier
	s_cbranch_vccnz .LBB0_880
	v_lshlrev_b32_e32 v0, 2, v218
	v_add_u32_e32 v1, 0, v0
	v_add_u32_e32 v1, 0x18100, v1
	ds_read_b32 v222, v1
	s_add_i32 s0, 0, 0x18200
	v_lshlrev_b32_e32 v1, 9, v219
	v_lshlrev_b32_e32 v2, 4, v218
	v_add_u32_e32 v224, s0, v0
	v_mov_b32_e32 v0, s27
	v_add3_u32 v223, s65, v1, v2
	v_lshlrev_b32_e32 v219, 2, v219
	v_lshl_add_u32 v225, v218, 11, 0
	v_cmp_gt_u32_e64 s[84:85], 32, v217
	v_mad_u32_u24 v217, v218, s24, v0
	v_readlane_b32 s0, v254, 24

; #define LAS __attribute__((address_space(3)))
; __device__ __forceinline__ bool run_unit2(LAS unsigned char* lds, const bf16* y0, const float* aux, unsigned* maskg, int b, int g, int tid_in, int wave, int lane) {
;     ...
;     __syncthreads();
;     {
;         const int q = tid >> 4, i = tid & 15;
;         const LAS unsigned long long* cq = (const LAS unsigned long long*)(lds + OFF2_CAND) + q * CAP2;
;         const int n = (int)((const LAS unsigned*)(lds + OFF2_CNT))[q], need = ((const LAS int*)(lds + OFF2_NEED))[q];
;         for (int a_ = i; a_ < n; a_ += 16) {
;             const unsigned long long mine = cq[a_];
;             int rank = 0;
;             const int n8 = (n + 7) & ~7;
;             for (int j = 0; j < n8; j += 8) {
.LBB0_880:
	s_waitcnt vmcnt(0)
	v_add_u32_e32 v0, 0x18200, v221
	s_waitcnt lgkmcnt(0)
	s_barrier
	ds_read_b32 v2, v0
	s_waitcnt lgkmcnt(0)
	v_cmp_lt_i32_e32 vcc, v216, v2
	s_and_saveexec_b64 s[4:5], vcc
	s_cbranch_execz .LBB0_887
	v_add_u32_e32 v0, 0x18180, v221
	ds_read_b32 v4, v0
	v_add_u32_e32 v0, 7, v2
	v_and_b32_e32 v5, -8, v0
	v_mul_lo_u32 v0, v220, s24
	v_lshl_add_u32 v3, v220, 11, 0
	v_add_u32_e32 v6, s27, v0
	s_mov_b64 s[6:7], 0
	s_branch .LBB0_883
